# speedup vs baseline: 1.0222x; 1.0029x over previous
.Lmk_start:
	s_mov_b32 s28, s8
	s_mov_b64 s[30:31], s[4:5]
	s_mov_b64 s[32:33], s[6:7]
	s_mov_b64 s[6:7], s[2:3]
	s_mov_b64 s[34:35], s[2:3]
	s_mov_b32 s2, s28
	s_and_b32 s3, s2, 7
	s_lshr_b32 s4, s2, 3
	s_and_b32 s5, s4, 3
	s_lshl_b32 s3, s3, 2
	s_or_b32 s8, s3, s5
	s_lshr_b32 s9, s4, 2
	v_lshrrev_b32_e32 v127, 6, v0
	v_and_b32_e32 v124, 63, v0
	v_lshlrev_b32_e32 v125, 3, v124
	v_lshlrev_b32_e32 v124, 4, v124
	v_readfirstlane_b32 s12, v127
	v_mov_b32_e32 v120, 0
	v_mov_b32_e32 v121, 0
	v_mov_b32_e32 v122, 0
	v_mov_b32_e32 v123, 0
	s_lshl_b32 s13, s12, 10
	s_lshl_b32 s14, s9, 3
	s_add_u32 s14, s14, s12
	s_mul_i32 s15, s14, 0x1800
	s_mul_i32 s16, s8, 0x12000
	s_add_u32 s16, s16, 0xc0000
	s_add_u32 s16, s16, s13
	s_add_u32 s20, s13, 0x2000
	s_add_u32 s10, s6, s16
	s_addc_u32 s11, s7, 0
	s_add_u32 s18, s6, s15
	s_addc_u32 s19, s7, 0
	s_add_u32 s22, s18, 0xc00
	s_addc_u32 s23, s19, 0
	s_cmp_lt_u32 s12, 4
	s_cbranch_scc0 .Lmk_vb
	s_mov_b32 m0, s13
	s_nop 0
	global_load_lds_dwordx4 v124, s[10:11]
	s_add_u32 s26, s10, 0x2000
	s_addc_u32 s27, s11, 0
	s_mov_b32 m0, s20
	s_nop 0
	global_load_lds_dwordx4 v124, s[26:27]
	global_load_dwordx4 v[96:99], v124, s[18:19]
	global_load_dwordx4 v[100:103], v124, s[18:19] offset:1024
	global_load_dwordx4 v[104:107], v124, s[18:19] offset:2048
	global_load_dwordx4 v[108:111], v124, s[22:23]
	global_load_dwordx4 v[112:115], v124, s[22:23] offset:1024
	global_load_dwordx4 v[116:119], v124, s[22:23] offset:2048
	s_add_u32 s24, s10, 0x3000
	s_addc_u32 s25, s11, 0
	s_add_u32 s26, s13, 0x3000
	s_mov_b32 m0, s26
	s_nop 0
	global_load_lds_dwordx4 v124, s[24:25]
	s_add_u32 s26, s24, 0x2000
	s_addc_u32 s27, s25, 0
	s_add_u32 s29, s20, 0x3000
	s_mov_b32 m0, s29
	s_nop 0
	global_load_lds_dwordx4 v124, s[26:27]
	s_add_u32 s24, s10, 0x6000
	s_addc_u32 s25, s11, 0
	s_add_u32 s26, s13, 0x6000
	s_mov_b32 m0, s26
	s_nop 0
	global_load_lds_dwordx4 v124, s[24:25]
	s_add_u32 s26, s24, 0x2000
	s_addc_u32 s27, s25, 0
	s_add_u32 s29, s20, 0x6000
	s_mov_b32 m0, s29
	s_nop 0
	global_load_lds_dwordx4 v124, s[26:27]
	s_add_u32 s24, s10, 0x9000
	s_addc_u32 s25, s11, 0
	s_add_u32 s26, s13, 0x9000
	s_mov_b32 m0, s26
	s_nop 0
	global_load_lds_dwordx4 v124, s[24:25]
	s_add_u32 s26, s24, 0x2000
	s_addc_u32 s27, s25, 0
	s_add_u32 s29, s20, 0x9000
	s_mov_b32 m0, s29
	s_nop 0
	global_load_lds_dwordx4 v124, s[26:27]
	s_add_u32 s24, s10, 0xc000
	s_addc_u32 s25, s11, 0
	s_add_u32 s26, s13, 0xc000
	s_mov_b32 m0, s26
	s_nop 0
	global_load_lds_dwordx4 v124, s[24:25]
	s_add_u32 s26, s24, 0x2000
	s_addc_u32 s27, s25, 0
	s_add_u32 s29, s20, 0xc000
	s_mov_b32 m0, s29
	s_nop 0
	global_load_lds_dwordx4 v124, s[26:27]
	s_waitcnt vmcnt(8)
	s_barrier
	ds_read_b128 v[0:3], v124
	ds_read_b128 v[4:7], v124 offset:1024
	ds_read_b128 v[8:11], v124 offset:2048
	ds_read_b128 v[12:15], v124 offset:3072
	ds_read_b128 v[16:19], v124 offset:4096
	ds_read_b128 v[20:23], v124 offset:5120
	s_waitcnt lgkmcnt(0)
	s_setprio 2
	v_mfma_f32_32x32x64_f8f6f4 v[48:63], v[0:5], v[96:101], 0 cbsz:2 blgp:2
	ds_read_b128 v[24:27], v124 offset:6144
	v_mfma_f32_32x32x64_f8f6f4 v[48:63], v[6:11], v[102:107], v[48:63] cbsz:2 blgp:2
	ds_read_b128 v[28:31], v124 offset:7168
	ds_read_b128 v[32:35], v124 offset:8192
	v_mfma_f32_32x32x64_f8f6f4 v[48:63], v[12:17], v[108:113], v[48:63] cbsz:2 blgp:2
	ds_read_b128 v[36:39], v124 offset:9216
	v_mfma_f32_32x32x64_f8f6f4 v[48:63], v[18:23], v[114:119], v[48:63] cbsz:2 blgp:2
	ds_read_b128 v[40:43], v124 offset:10240
	ds_read_b128 v[44:47], v124 offset:11264
	s_waitcnt vmcnt(0) lgkmcnt(0)
	s_barrier
	s_add_u32 s24, s10, 0xf000
	s_addc_u32 s25, s11, 0
	s_mov_b32 m0, s13
	s_nop 0
	global_load_lds_dwordx4 v124, s[24:25]
	s_add_u32 s26, s24, 0x2000
	s_addc_u32 s27, s25, 0
	s_mov_b32 m0, s20
	s_nop 0
	global_load_lds_dwordx4 v124, s[26:27]
	v_mfma_f32_32x32x64_f8f6f4 v[64:79], v[24:29], v[96:101], 0 cbsz:2 blgp:2
	ds_read_b128 v[0:3], v124 offset:12288
	ds_read_b128 v[4:7], v124 offset:13312
	ds_read_b128 v[8:11], v124 offset:14336
	ds_read_b128 v[24:27], v124 offset:18432
	v_mfma_f32_32x32x64_f8f6f4 v[64:79], v[30:35], v[102:107], v[64:79] cbsz:2 blgp:2
	ds_read_b128 v[12:15], v124 offset:15360
	ds_read_b128 v[16:19], v124 offset:16384
	ds_read_b128 v[20:23], v124 offset:17408
	ds_read_b128 v[28:31], v124 offset:19456
	ds_read_b128 v[32:35], v124 offset:20480
	v_exp_f32_e32 v48, v48
	v_exp_f32_e32 v49, v49
	v_exp_f32_e32 v50, v50
	v_exp_f32_e32 v51, v51
	v_mfma_f32_32x32x64_f8f6f4 v[64:79], v[36:41], v[108:113], v[64:79] cbsz:2 blgp:2
	ds_read_b128 v[36:39], v124 offset:21504
	v_exp_f32_e32 v52, v52
	v_exp_f32_e32 v53, v53
	v_exp_f32_e32 v54, v54
	v_exp_f32_e32 v55, v55
	v_pk_add_f32 v[120:121], v[120:121], v[48:49]
	v_pk_add_f32 v[122:123], v[122:123], v[50:51]
	v_mfma_f32_32x32x64_f8f6f4 v[64:79], v[42:47], v[114:119], v[64:79] cbsz:2 blgp:2
	ds_read_b128 v[40:43], v124 offset:22528
	ds_read_b128 v[44:47], v124 offset:23552
	v_exp_f32_e32 v56, v56
	v_exp_f32_e32 v57, v57
	v_exp_f32_e32 v58, v58
	v_exp_f32_e32 v59, v59
	v_pk_add_f32 v[120:121], v[120:121], v[52:53]
	v_pk_add_f32 v[122:123], v[122:123], v[54:55]
	s_waitcnt lgkmcnt(5)
	v_mfma_f32_32x32x64_f8f6f4 v[80:95], v[0:5], v[96:101], 0 cbsz:2 blgp:2
	ds_read_b128 v[0:3], v124 offset:24576
	v_exp_f32_e32 v60, v60
	v_exp_f32_e32 v61, v61
	v_exp_f32_e32 v62, v62
	v_exp_f32_e32 v63, v63
	v_pk_add_f32 v[120:121], v[120:121], v[56:57]
	v_pk_add_f32 v[122:123], v[122:123], v[58:59]
	v_mfma_f32_32x32x64_f8f6f4 v[80:95], v[6:11], v[102:107], v[80:95] cbsz:2 blgp:2
	ds_read_b128 v[4:7], v124 offset:25600
	ds_read_b128 v[8:11], v124 offset:26624
	v_exp_f32_e32 v64, v64
	v_exp_f32_e32 v65, v65
	v_exp_f32_e32 v66, v66
	v_exp_f32_e32 v67, v67
	v_pk_add_f32 v[120:121], v[120:121], v[60:61]
	v_pk_add_f32 v[122:123], v[122:123], v[62:63]
	v_mfma_f32_32x32x64_f8f6f4 v[80:95], v[12:17], v[108:113], v[80:95] cbsz:2 blgp:2
	ds_read_b128 v[12:15], v124 offset:27648
	v_exp_f32_e32 v68, v68
	v_exp_f32_e32 v69, v69
	v_exp_f32_e32 v70, v70
	v_exp_f32_e32 v71, v71
	v_pk_add_f32 v[120:121], v[120:121], v[64:65]
	v_pk_add_f32 v[122:123], v[122:123], v[66:67]
	v_mfma_f32_32x32x64_f8f6f4 v[80:95], v[18:23], v[114:119], v[80:95] cbsz:2 blgp:2
	ds_read_b128 v[16:19], v124 offset:28672
	ds_read_b128 v[20:23], v124 offset:29696
	v_exp_f32_e32 v72, v72
	v_exp_f32_e32 v73, v73
	v_exp_f32_e32 v74, v74
	v_exp_f32_e32 v75, v75
	v_pk_add_f32 v[120:121], v[120:121], v[68:69]
	v_pk_add_f32 v[122:123], v[122:123], v[70:71]
	s_waitcnt lgkmcnt(6)
	v_mfma_f32_32x32x64_f8f6f4 v[48:63], v[24:29], v[96:101], 0 cbsz:2 blgp:2
	ds_read_b128 v[24:27], v124 offset:30720
	v_exp_f32_e32 v76, v76
	v_exp_f32_e32 v77, v77
	v_exp_f32_e32 v78, v78
	v_exp_f32_e32 v79, v79
	v_pk_add_f32 v[120:121], v[120:121], v[72:73]
	v_pk_add_f32 v[122:123], v[122:123], v[74:75]
	v_mfma_f32_32x32x64_f8f6f4 v[48:63], v[30:35], v[102:107], v[48:63] cbsz:2 blgp:2
	ds_read_b128 v[28:31], v124 offset:31744
	ds_read_b128 v[32:35], v124 offset:32768
	v_exp_f32_e32 v80, v80
	v_exp_f32_e32 v81, v81
	v_exp_f32_e32 v82, v82
	v_exp_f32_e32 v83, v83
	v_pk_add_f32 v[120:121], v[120:121], v[76:77]
	v_pk_add_f32 v[122:123], v[122:123], v[78:79]
	v_mfma_f32_32x32x64_f8f6f4 v[48:63], v[36:41], v[108:113], v[48:63] cbsz:2 blgp:2
	ds_read_b128 v[36:39], v124 offset:33792
	v_exp_f32_e32 v84, v84
	v_exp_f32_e32 v85, v85
	v_exp_f32_e32 v86, v86
	v_exp_f32_e32 v87, v87
	v_pk_add_f32 v[120:121], v[120:121], v[80:81]
	v_pk_add_f32 v[122:123], v[122:123], v[82:83]
	v_mfma_f32_32x32x64_f8f6f4 v[48:63], v[42:47], v[114:119], v[48:63] cbsz:2 blgp:2
	ds_read_b128 v[40:43], v124 offset:34816
	ds_read_b128 v[44:47], v124 offset:35840
	v_exp_f32_e32 v88, v88
	v_exp_f32_e32 v89, v89
	v_exp_f32_e32 v90, v90
	v_exp_f32_e32 v91, v91
	v_pk_add_f32 v[120:121], v[120:121], v[84:85]
	v_pk_add_f32 v[122:123], v[122:123], v[86:87]
	s_setprio 1
	s_waitcnt lgkmcnt(6)
	v_mfma_f32_32x32x64_f8f6f4 v[64:79], v[0:5], v[96:101], 0 cbsz:2 blgp:2
	ds_read_b128 v[0:3], v124 offset:36864
	v_exp_f32_e32 v92, v92
	v_exp_f32_e32 v93, v93
	v_exp_f32_e32 v94, v94
	v_exp_f32_e32 v95, v95
	v_pk_add_f32 v[120:121], v[120:121], v[88:89]
	v_pk_add_f32 v[122:123], v[122:123], v[90:91]
	v_mfma_f32_32x32x64_f8f6f4 v[64:79], v[6:11], v[102:107], v[64:79] cbsz:2 blgp:2
	ds_read_b128 v[4:7], v124 offset:37888
	ds_read_b128 v[8:11], v124 offset:38912
	v_exp_f32_e32 v48, v48
	v_exp_f32_e32 v49, v49
	v_exp_f32_e32 v50, v50
	v_exp_f32_e32 v51, v51
	v_pk_add_f32 v[120:121], v[120:121], v[92:93]
	v_pk_add_f32 v[122:123], v[122:123], v[94:95]
	v_mfma_f32_32x32x64_f8f6f4 v[64:79], v[12:17], v[108:113], v[64:79] cbsz:2 blgp:2
	ds_read_b128 v[12:15], v124 offset:39936
	v_exp_f32_e32 v52, v52
	v_exp_f32_e32 v53, v53
	v_exp_f32_e32 v54, v54
	v_exp_f32_e32 v55, v55
	v_pk_add_f32 v[120:121], v[120:121], v[48:49]
	v_pk_add_f32 v[122:123], v[122:123], v[50:51]
	v_mfma_f32_32x32x64_f8f6f4 v[64:79], v[18:23], v[114:119], v[64:79] cbsz:2 blgp:2
	ds_read_b128 v[16:19], v124 offset:40960
	ds_read_b128 v[20:23], v124 offset:41984
	v_exp_f32_e32 v56, v56
	v_exp_f32_e32 v57, v57
	v_exp_f32_e32 v58, v58
	v_exp_f32_e32 v59, v59
	v_pk_add_f32 v[120:121], v[120:121], v[52:53]
	v_pk_add_f32 v[122:123], v[122:123], v[54:55]
	s_waitcnt lgkmcnt(6)
	v_mfma_f32_32x32x64_f8f6f4 v[80:95], v[24:29], v[96:101], 0 cbsz:2 blgp:2
	ds_read_b128 v[24:27], v124 offset:43008
	v_exp_f32_e32 v60, v60
	v_exp_f32_e32 v61, v61
	v_exp_f32_e32 v62, v62
	v_exp_f32_e32 v63, v63
	v_pk_add_f32 v[120:121], v[120:121], v[56:57]
	v_pk_add_f32 v[122:123], v[122:123], v[58:59]
	v_mfma_f32_32x32x64_f8f6f4 v[80:95], v[30:35], v[102:107], v[80:95] cbsz:2 blgp:2
	ds_read_b128 v[28:31], v124 offset:44032
	ds_read_b128 v[32:35], v124 offset:45056
	v_exp_f32_e32 v64, v64
	v_exp_f32_e32 v65, v65
	v_exp_f32_e32 v66, v66
	v_exp_f32_e32 v67, v67
	v_pk_add_f32 v[120:121], v[120:121], v[60:61]
	v_pk_add_f32 v[122:123], v[122:123], v[62:63]
	v_mfma_f32_32x32x64_f8f6f4 v[80:95], v[36:41], v[108:113], v[80:95] cbsz:2 blgp:2
	ds_read_b128 v[36:39], v124 offset:46080
	v_exp_f32_e32 v68, v68
	v_exp_f32_e32 v69, v69
	v_exp_f32_e32 v70, v70
	v_exp_f32_e32 v71, v71
	v_pk_add_f32 v[120:121], v[120:121], v[64:65]
	v_pk_add_f32 v[122:123], v[122:123], v[66:67]
	v_mfma_f32_32x32x64_f8f6f4 v[80:95], v[42:47], v[114:119], v[80:95] cbsz:2 blgp:2
	ds_read_b128 v[40:43], v124 offset:47104
	ds_read_b128 v[44:47], v124 offset:48128
	v_exp_f32_e32 v72, v72
	v_exp_f32_e32 v73, v73
	v_exp_f32_e32 v74, v74
	v_exp_f32_e32 v75, v75
	v_pk_add_f32 v[120:121], v[120:121], v[68:69]
	v_pk_add_f32 v[122:123], v[122:123], v[70:71]
	s_waitcnt lgkmcnt(6)
	v_mfma_f32_32x32x64_f8f6f4 v[48:63], v[0:5], v[96:101], 0 cbsz:2 blgp:2
	ds_read_b128 v[0:3], v124 offset:49152
	v_exp_f32_e32 v76, v76
	v_exp_f32_e32 v77, v77
	v_exp_f32_e32 v78, v78
	v_exp_f32_e32 v79, v79
	v_pk_add_f32 v[120:121], v[120:121], v[72:73]
	v_pk_add_f32 v[122:123], v[122:123], v[74:75]
	v_mfma_f32_32x32x64_f8f6f4 v[48:63], v[6:11], v[102:107], v[48:63] cbsz:2 blgp:2
	ds_read_b128 v[4:7], v124 offset:50176
	ds_read_b128 v[8:11], v124 offset:51200
	v_exp_f32_e32 v80, v80
	v_exp_f32_e32 v81, v81
	v_exp_f32_e32 v82, v82
	v_exp_f32_e32 v83, v83
	v_pk_add_f32 v[120:121], v[120:121], v[76:77]
	v_pk_add_f32 v[122:123], v[122:123], v[78:79]
	v_mfma_f32_32x32x64_f8f6f4 v[48:63], v[12:17], v[108:113], v[48:63] cbsz:2 blgp:2
	ds_read_b128 v[12:15], v124 offset:52224
	v_exp_f32_e32 v84, v84
	v_exp_f32_e32 v85, v85
	v_exp_f32_e32 v86, v86
	v_exp_f32_e32 v87, v87
	v_pk_add_f32 v[120:121], v[120:121], v[80:81]
	v_pk_add_f32 v[122:123], v[122:123], v[82:83]
	v_mfma_f32_32x32x64_f8f6f4 v[48:63], v[18:23], v[114:119], v[48:63] cbsz:2 blgp:2
	ds_read_b128 v[16:19], v124 offset:53248
	ds_read_b128 v[20:23], v124 offset:54272
	v_exp_f32_e32 v88, v88
	v_exp_f32_e32 v89, v89
	v_exp_f32_e32 v90, v90
	v_exp_f32_e32 v91, v91
	v_pk_add_f32 v[120:121], v[120:121], v[84:85]
	v_pk_add_f32 v[122:123], v[122:123], v[86:87]
	s_waitcnt lgkmcnt(6)
	v_mfma_f32_32x32x64_f8f6f4 v[64:79], v[24:29], v[96:101], 0 cbsz:2 blgp:2
	ds_read_b128 v[24:27], v124 offset:55296
	v_exp_f32_e32 v92, v92
	v_exp_f32_e32 v93, v93
	v_exp_f32_e32 v94, v94
	v_exp_f32_e32 v95, v95
	v_pk_add_f32 v[120:121], v[120:121], v[88:89]
	v_pk_add_f32 v[122:123], v[122:123], v[90:91]
	v_mfma_f32_32x32x64_f8f6f4 v[64:79], v[30:35], v[102:107], v[64:79] cbsz:2 blgp:2
	ds_read_b128 v[28:31], v124 offset:56320
	ds_read_b128 v[32:35], v124 offset:57344
	v_exp_f32_e32 v48, v48
	v_exp_f32_e32 v49, v49
	v_exp_f32_e32 v50, v50
	v_exp_f32_e32 v51, v51
	v_pk_add_f32 v[120:121], v[120:121], v[92:93]
	v_pk_add_f32 v[122:123], v[122:123], v[94:95]
	v_mfma_f32_32x32x64_f8f6f4 v[64:79], v[36:41], v[108:113], v[64:79] cbsz:2 blgp:2
	ds_read_b128 v[36:39], v124 offset:58368
	v_exp_f32_e32 v52, v52
	v_exp_f32_e32 v53, v53
	v_exp_f32_e32 v54, v54
	v_exp_f32_e32 v55, v55
	v_pk_add_f32 v[120:121], v[120:121], v[48:49]
	v_pk_add_f32 v[122:123], v[122:123], v[50:51]
	v_mfma_f32_32x32x64_f8f6f4 v[64:79], v[42:47], v[114:119], v[64:79] cbsz:2 blgp:2
	ds_read_b128 v[40:43], v124 offset:59392
	ds_read_b128 v[44:47], v124 offset:60416
	v_exp_f32_e32 v56, v56
	v_exp_f32_e32 v57, v57
	v_exp_f32_e32 v58, v58
	v_exp_f32_e32 v59, v59
	v_pk_add_f32 v[120:121], v[120:121], v[52:53]
	v_pk_add_f32 v[122:123], v[122:123], v[54:55]
	s_setprio 0
	s_waitcnt vmcnt(0) lgkmcnt(6)
	s_barrier
	v_mfma_f32_32x32x64_f8f6f4 v[80:95], v[0:5], v[96:101], 0 cbsz:2 blgp:2
	ds_read_b128 v[0:3], v124
	v_exp_f32_e32 v60, v60
	v_exp_f32_e32 v61, v61
	v_exp_f32_e32 v62, v62
	v_exp_f32_e32 v63, v63
	v_pk_add_f32 v[120:121], v[120:121], v[56:57]
	v_pk_add_f32 v[122:123], v[122:123], v[58:59]
	v_mfma_f32_32x32x64_f8f6f4 v[80:95], v[6:11], v[102:107], v[80:95] cbsz:2 blgp:2
	ds_read_b128 v[4:7], v124 offset:1024
	ds_read_b128 v[8:11], v124 offset:2048
	v_exp_f32_e32 v64, v64
	v_exp_f32_e32 v65, v65
	v_exp_f32_e32 v66, v66
	v_exp_f32_e32 v67, v67
	v_pk_add_f32 v[120:121], v[120:121], v[60:61]
	v_pk_add_f32 v[122:123], v[122:123], v[62:63]
	v_mfma_f32_32x32x64_f8f6f4 v[80:95], v[12:17], v[108:113], v[80:95] cbsz:2 blgp:2
	ds_read_b128 v[12:15], v124 offset:3072
	v_exp_f32_e32 v68, v68
	v_exp_f32_e32 v69, v69
	v_exp_f32_e32 v70, v70
	v_exp_f32_e32 v71, v71
	v_pk_add_f32 v[120:121], v[120:121], v[64:65]
	v_pk_add_f32 v[122:123], v[122:123], v[66:67]
	v_mfma_f32_32x32x64_f8f6f4 v[80:95], v[18:23], v[114:119], v[80:95] cbsz:2 blgp:2
	ds_read_b128 v[16:19], v124 offset:4096
	ds_read_b128 v[20:23], v124 offset:5120
	v_exp_f32_e32 v72, v72
	v_exp_f32_e32 v73, v73
	v_exp_f32_e32 v74, v74
	v_exp_f32_e32 v75, v75
	v_pk_add_f32 v[120:121], v[120:121], v[68:69]
	v_pk_add_f32 v[122:123], v[122:123], v[70:71]
	s_waitcnt lgkmcnt(6)
	v_mfma_f32_32x32x64_f8f6f4 v[48:63], v[24:29], v[96:101], 0 cbsz:2 blgp:2
	ds_read_b128 v[24:27], v124 offset:6144
	v_exp_f32_e32 v76, v76
	v_exp_f32_e32 v77, v77
	v_exp_f32_e32 v78, v78
	v_exp_f32_e32 v79, v79
	v_pk_add_f32 v[120:121], v[120:121], v[72:73]
	v_pk_add_f32 v[122:123], v[122:123], v[74:75]
	v_mfma_f32_32x32x64_f8f6f4 v[48:63], v[30:35], v[102:107], v[48:63] cbsz:2 blgp:2
	ds_read_b128 v[28:31], v124 offset:7168
	ds_read_b128 v[32:35], v124 offset:8192
	v_exp_f32_e32 v80, v80
	v_exp_f32_e32 v81, v81
	v_exp_f32_e32 v82, v82
	v_exp_f32_e32 v83, v83
	v_pk_add_f32 v[120:121], v[120:121], v[76:77]
	v_pk_add_f32 v[122:123], v[122:123], v[78:79]
	s_cmp_lg_u32 s8, 10
	s_cbranch_scc1 .Lmk_nosplit_a
	v_add_f32_e32 v127, v120, v121
	v_add_f32_e32 v126, v122, v123
	v_mov_b32_e32 v120, 0
	v_mov_b32_e32 v121, 0
	v_mov_b32_e32 v122, 0
	v_mov_b32_e32 v123, 0
	v_add_f32_e32 v127, v127, v126

.Lmk_vb:
	s_mov_b32 m0, s13
	s_nop 0
	global_load_lds_dwordx4 v124, s[10:11]
	global_load_dwordx4 v[96:99], v124, s[18:19]
	global_load_dwordx4 v[100:103], v124, s[18:19] offset:1024
	global_load_dwordx4 v[104:107], v124, s[18:19] offset:2048
	global_load_dwordx4 v[108:111], v124, s[22:23]
	global_load_dwordx4 v[112:115], v124, s[22:23] offset:1024
	global_load_dwordx4 v[116:119], v124, s[22:23] offset:2048
	s_add_u32 s24, s10, 0x3000
	s_addc_u32 s25, s11, 0
	s_add_u32 s26, s13, 0x3000
	s_mov_b32 m0, s26
	s_nop 0
	global_load_lds_dwordx4 v124, s[24:25]
	s_add_u32 s24, s10, 0x6000
	s_addc_u32 s25, s11, 0
	s_add_u32 s26, s13, 0x6000
	s_mov_b32 m0, s26
	s_nop 0
	global_load_lds_dwordx4 v124, s[24:25]
	s_add_u32 s24, s10, 0x9000
	s_addc_u32 s25, s11, 0
	s_add_u32 s26, s13, 0x9000
	s_mov_b32 m0, s26
	s_nop 0
	global_load_lds_dwordx4 v124, s[24:25]
	s_add_u32 s24, s10, 0xc000
	s_addc_u32 s25, s11, 0
	s_add_u32 s26, s13, 0xc000
	s_mov_b32 m0, s26
	s_nop 0
	global_load_lds_dwordx4 v124, s[24:25]
	s_waitcnt vmcnt(4)
	s_barrier
	ds_read_b128 v[0:3], v124
	ds_read_b128 v[4:7], v124 offset:1024
	ds_read_b128 v[8:11], v124 offset:2048
	ds_read_b128 v[12:15], v124 offset:3072
	ds_read_b128 v[16:19], v124 offset:4096
	ds_read_b128 v[20:23], v124 offset:5120
	s_waitcnt lgkmcnt(0)
	s_setprio 3
	v_mfma_f32_32x32x64_f8f6f4 v[48:63], v[0:5], v[96:101], 0 cbsz:2 blgp:2
	ds_read_b128 v[24:27], v124 offset:6144
	v_mfma_f32_32x32x64_f8f6f4 v[48:63], v[6:11], v[102:107], v[48:63] cbsz:2 blgp:2
	ds_read_b128 v[28:31], v124 offset:7168
	ds_read_b128 v[32:35], v124 offset:8192
	v_mfma_f32_32x32x64_f8f6f4 v[48:63], v[12:17], v[108:113], v[48:63] cbsz:2 blgp:2
	ds_read_b128 v[36:39], v124 offset:9216
	v_mfma_f32_32x32x64_f8f6f4 v[48:63], v[18:23], v[114:119], v[48:63] cbsz:2 blgp:2
	ds_read_b128 v[40:43], v124 offset:10240
	ds_read_b128 v[44:47], v124 offset:11264
	s_waitcnt vmcnt(0) lgkmcnt(0)
	s_barrier
	s_add_u32 s24, s10, 0xf000
	s_addc_u32 s25, s11, 0
	s_mov_b32 m0, s13
	s_nop 0
	global_load_lds_dwordx4 v124, s[24:25]
	v_mfma_f32_32x32x64_f8f6f4 v[64:79], v[24:29], v[96:101], 0 cbsz:2 blgp:2
	ds_read_b128 v[0:3], v124 offset:12288
	ds_read_b128 v[4:7], v124 offset:13312
	ds_read_b128 v[8:11], v124 offset:14336
	ds_read_b128 v[24:27], v124 offset:18432
	v_mfma_f32_32x32x64_f8f6f4 v[64:79], v[30:35], v[102:107], v[64:79] cbsz:2 blgp:2
	ds_read_b128 v[12:15], v124 offset:15360
	ds_read_b128 v[16:19], v124 offset:16384
	ds_read_b128 v[20:23], v124 offset:17408
	ds_read_b128 v[28:31], v124 offset:19456
	ds_read_b128 v[32:35], v124 offset:20480
	v_exp_f32_e32 v48, v48
	v_exp_f32_e32 v49, v49
	v_exp_f32_e32 v50, v50
	v_exp_f32_e32 v51, v51
	v_mfma_f32_32x32x64_f8f6f4 v[64:79], v[36:41], v[108:113], v[64:79] cbsz:2 blgp:2
	ds_read_b128 v[36:39], v124 offset:21504
	v_exp_f32_e32 v52, v52
	v_exp_f32_e32 v53, v53
	v_exp_f32_e32 v54, v54
	v_exp_f32_e32 v55, v55
	v_pk_add_f32 v[120:121], v[120:121], v[48:49]
	v_pk_add_f32 v[122:123], v[122:123], v[50:51]
	v_mfma_f32_32x32x64_f8f6f4 v[64:79], v[42:47], v[114:119], v[64:79] cbsz:2 blgp:2
	ds_read_b128 v[40:43], v124 offset:22528
	ds_read_b128 v[44:47], v124 offset:23552
	v_exp_f32_e32 v56, v56
	v_exp_f32_e32 v57, v57
	v_exp_f32_e32 v58, v58
	v_exp_f32_e32 v59, v59
	v_pk_add_f32 v[120:121], v[120:121], v[52:53]
	v_pk_add_f32 v[122:123], v[122:123], v[54:55]
	s_waitcnt lgkmcnt(5)
	v_mfma_f32_32x32x64_f8f6f4 v[80:95], v[0:5], v[96:101], 0 cbsz:2 blgp:2
	ds_read_b128 v[0:3], v124 offset:24576
	v_exp_f32_e32 v60, v60
	v_exp_f32_e32 v61, v61
	v_exp_f32_e32 v62, v62
	v_exp_f32_e32 v63, v63
	v_pk_add_f32 v[120:121], v[120:121], v[56:57]
	v_pk_add_f32 v[122:123], v[122:123], v[58:59]
	v_mfma_f32_32x32x64_f8f6f4 v[80:95], v[6:11], v[102:107], v[80:95] cbsz:2 blgp:2
	ds_read_b128 v[4:7], v124 offset:25600
	ds_read_b128 v[8:11], v124 offset:26624
	v_exp_f32_e32 v64, v64
	v_exp_f32_e32 v65, v65
	v_exp_f32_e32 v66, v66
	v_exp_f32_e32 v67, v67
	v_pk_add_f32 v[120:121], v[120:121], v[60:61]
	v_pk_add_f32 v[122:123], v[122:123], v[62:63]
	v_mfma_f32_32x32x64_f8f6f4 v[80:95], v[12:17], v[108:113], v[80:95] cbsz:2 blgp:2
	ds_read_b128 v[12:15], v124 offset:27648
	v_exp_f32_e32 v68, v68
	v_exp_f32_e32 v69, v69
	v_exp_f32_e32 v70, v70
	v_exp_f32_e32 v71, v71
	v_pk_add_f32 v[120:121], v[120:121], v[64:65]
	v_pk_add_f32 v[122:123], v[122:123], v[66:67]
	v_mfma_f32_32x32x64_f8f6f4 v[80:95], v[18:23], v[114:119], v[80:95] cbsz:2 blgp:2
	ds_read_b128 v[16:19], v124 offset:28672
	ds_read_b128 v[20:23], v124 offset:29696
	v_exp_f32_e32 v72, v72
	v_exp_f32_e32 v73, v73
	v_exp_f32_e32 v74, v74
	v_exp_f32_e32 v75, v75
	v_pk_add_f32 v[120:121], v[120:121], v[68:69]
	v_pk_add_f32 v[122:123], v[122:123], v[70:71]
	s_waitcnt lgkmcnt(6)
	v_mfma_f32_32x32x64_f8f6f4 v[48:63], v[24:29], v[96:101], 0 cbsz:2 blgp:2
	ds_read_b128 v[24:27], v124 offset:30720
	v_exp_f32_e32 v76, v76
	v_exp_f32_e32 v77, v77
	v_exp_f32_e32 v78, v78
	v_exp_f32_e32 v79, v79
	v_pk_add_f32 v[120:121], v[120:121], v[72:73]
	v_pk_add_f32 v[122:123], v[122:123], v[74:75]
	v_mfma_f32_32x32x64_f8f6f4 v[48:63], v[30:35], v[102:107], v[48:63] cbsz:2 blgp:2
	ds_read_b128 v[28:31], v124 offset:31744
	ds_read_b128 v[32:35], v124 offset:32768
	v_exp_f32_e32 v80, v80
	v_exp_f32_e32 v81, v81
	v_exp_f32_e32 v82, v82
	v_exp_f32_e32 v83, v83
	v_pk_add_f32 v[120:121], v[120:121], v[76:77]
	v_pk_add_f32 v[122:123], v[122:123], v[78:79]
	v_mfma_f32_32x32x64_f8f6f4 v[48:63], v[36:41], v[108:113], v[48:63] cbsz:2 blgp:2
	ds_read_b128 v[36:39], v124 offset:33792
	v_exp_f32_e32 v84, v84
	v_exp_f32_e32 v85, v85
	v_exp_f32_e32 v86, v86
	v_exp_f32_e32 v87, v87
	v_pk_add_f32 v[120:121], v[120:121], v[80:81]
	v_pk_add_f32 v[122:123], v[122:123], v[82:83]
	v_mfma_f32_32x32x64_f8f6f4 v[48:63], v[42:47], v[114:119], v[48:63] cbsz:2 blgp:2
	ds_read_b128 v[40:43], v124 offset:34816
	ds_read_b128 v[44:47], v124 offset:35840
	v_exp_f32_e32 v88, v88
	v_exp_f32_e32 v89, v89
	v_exp_f32_e32 v90, v90
	v_exp_f32_e32 v91, v91
	v_pk_add_f32 v[120:121], v[120:121], v[84:85]
	v_pk_add_f32 v[122:123], v[122:123], v[86:87]
	s_setprio 2
	s_waitcnt lgkmcnt(6)
	v_mfma_f32_32x32x64_f8f6f4 v[64:79], v[0:5], v[96:101], 0 cbsz:2 blgp:2
	ds_read_b128 v[0:3], v124 offset:36864
	v_exp_f32_e32 v92, v92
	v_exp_f32_e32 v93, v93
	v_exp_f32_e32 v94, v94
	v_exp_f32_e32 v95, v95
	v_pk_add_f32 v[120:121], v[120:121], v[88:89]
	v_pk_add_f32 v[122:123], v[122:123], v[90:91]
	v_mfma_f32_32x32x64_f8f6f4 v[64:79], v[6:11], v[102:107], v[64:79] cbsz:2 blgp:2
	ds_read_b128 v[4:7], v124 offset:37888
	ds_read_b128 v[8:11], v124 offset:38912
	v_exp_f32_e32 v48, v48
	v_exp_f32_e32 v49, v49
	v_exp_f32_e32 v50, v50
	v_exp_f32_e32 v51, v51
	v_pk_add_f32 v[120:121], v[120:121], v[92:93]
	v_pk_add_f32 v[122:123], v[122:123], v[94:95]
	v_mfma_f32_32x32x64_f8f6f4 v[64:79], v[12:17], v[108:113], v[64:79] cbsz:2 blgp:2
	ds_read_b128 v[12:15], v124 offset:39936
	v_exp_f32_e32 v52, v52
	v_exp_f32_e32 v53, v53
	v_exp_f32_e32 v54, v54
	v_exp_f32_e32 v55, v55
	v_pk_add_f32 v[120:121], v[120:121], v[48:49]
	v_pk_add_f32 v[122:123], v[122:123], v[50:51]
	v_mfma_f32_32x32x64_f8f6f4 v[64:79], v[18:23], v[114:119], v[64:79] cbsz:2 blgp:2
	ds_read_b128 v[16:19], v124 offset:40960
	ds_read_b128 v[20:23], v124 offset:41984
	v_exp_f32_e32 v56, v56
	v_exp_f32_e32 v57, v57
	v_exp_f32_e32 v58, v58
	v_exp_f32_e32 v59, v59
	v_pk_add_f32 v[120:121], v[120:121], v[52:53]
	v_pk_add_f32 v[122:123], v[122:123], v[54:55]
	s_waitcnt lgkmcnt(6)
	v_mfma_f32_32x32x64_f8f6f4 v[80:95], v[24:29], v[96:101], 0 cbsz:2 blgp:2
	ds_read_b128 v[24:27], v124 offset:43008
	v_exp_f32_e32 v60, v60
	v_exp_f32_e32 v61, v61
	v_exp_f32_e32 v62, v62
	v_exp_f32_e32 v63, v63
	v_pk_add_f32 v[120:121], v[120:121], v[56:57]
	v_pk_add_f32 v[122:123], v[122:123], v[58:59]
	v_mfma_f32_32x32x64_f8f6f4 v[80:95], v[30:35], v[102:107], v[80:95] cbsz:2 blgp:2
	ds_read_b128 v[28:31], v124 offset:44032
	ds_read_b128 v[32:35], v124 offset:45056
	v_exp_f32_e32 v64, v64
	v_exp_f32_e32 v65, v65
	v_exp_f32_e32 v66, v66
	v_exp_f32_e32 v67, v67
	v_pk_add_f32 v[120:121], v[120:121], v[60:61]
	v_pk_add_f32 v[122:123], v[122:123], v[62:63]
	v_mfma_f32_32x32x64_f8f6f4 v[80:95], v[36:41], v[108:113], v[80:95] cbsz:2 blgp:2
	ds_read_b128 v[36:39], v124 offset:46080
	v_exp_f32_e32 v68, v68
	v_exp_f32_e32 v69, v69
	v_exp_f32_e32 v70, v70
	v_exp_f32_e32 v71, v71
	v_pk_add_f32 v[120:121], v[120:121], v[64:65]
	v_pk_add_f32 v[122:123], v[122:123], v[66:67]
	v_mfma_f32_32x32x64_f8f6f4 v[80:95], v[42:47], v[114:119], v[80:95] cbsz:2 blgp:2
	ds_read_b128 v[40:43], v124 offset:47104
	ds_read_b128 v[44:47], v124 offset:48128
	v_exp_f32_e32 v72, v72
	v_exp_f32_e32 v73, v73
	v_exp_f32_e32 v74, v74
	v_exp_f32_e32 v75, v75
	v_pk_add_f32 v[120:121], v[120:121], v[68:69]
	v_pk_add_f32 v[122:123], v[122:123], v[70:71]
	s_waitcnt lgkmcnt(6)
	v_mfma_f32_32x32x64_f8f6f4 v[48:63], v[0:5], v[96:101], 0 cbsz:2 blgp:2
	ds_read_b128 v[0:3], v124 offset:49152
	v_exp_f32_e32 v76, v76
	v_exp_f32_e32 v77, v77
	v_exp_f32_e32 v78, v78
	v_exp_f32_e32 v79, v79
	v_pk_add_f32 v[120:121], v[120:121], v[72:73]
	v_pk_add_f32 v[122:123], v[122:123], v[74:75]
	v_mfma_f32_32x32x64_f8f6f4 v[48:63], v[6:11], v[102:107], v[48:63] cbsz:2 blgp:2
	ds_read_b128 v[4:7], v124 offset:50176
	ds_read_b128 v[8:11], v124 offset:51200
	v_exp_f32_e32 v80, v80
	v_exp_f32_e32 v81, v81
	v_exp_f32_e32 v82, v82
	v_exp_f32_e32 v83, v83
	v_pk_add_f32 v[120:121], v[120:121], v[76:77]
	v_pk_add_f32 v[122:123], v[122:123], v[78:79]
	v_mfma_f32_32x32x64_f8f6f4 v[48:63], v[12:17], v[108:113], v[48:63] cbsz:2 blgp:2
	ds_read_b128 v[12:15], v124 offset:52224
	v_exp_f32_e32 v84, v84
	v_exp_f32_e32 v85, v85
	v_exp_f32_e32 v86, v86
	v_exp_f32_e32 v87, v87
	v_pk_add_f32 v[120:121], v[120:121], v[80:81]
	v_pk_add_f32 v[122:123], v[122:123], v[82:83]
	v_mfma_f32_32x32x64_f8f6f4 v[48:63], v[18:23], v[114:119], v[48:63] cbsz:2 blgp:2
	ds_read_b128 v[16:19], v124 offset:53248
	ds_read_b128 v[20:23], v124 offset:54272
	v_exp_f32_e32 v88, v88
	v_exp_f32_e32 v89, v89
	v_exp_f32_e32 v90, v90
	v_exp_f32_e32 v91, v91
	v_pk_add_f32 v[120:121], v[120:121], v[84:85]
	v_pk_add_f32 v[122:123], v[122:123], v[86:87]
	s_waitcnt lgkmcnt(6)
	v_mfma_f32_32x32x64_f8f6f4 v[64:79], v[24:29], v[96:101], 0 cbsz:2 blgp:2
	ds_read_b128 v[24:27], v124 offset:55296
	v_exp_f32_e32 v92, v92
	v_exp_f32_e32 v93, v93
	v_exp_f32_e32 v94, v94
	v_exp_f32_e32 v95, v95
	v_pk_add_f32 v[120:121], v[120:121], v[88:89]
	v_pk_add_f32 v[122:123], v[122:123], v[90:91]
	v_mfma_f32_32x32x64_f8f6f4 v[64:79], v[30:35], v[102:107], v[64:79] cbsz:2 blgp:2
	ds_read_b128 v[28:31], v124 offset:56320
	ds_read_b128 v[32:35], v124 offset:57344
	v_exp_f32_e32 v48, v48
	v_exp_f32_e32 v49, v49
	v_exp_f32_e32 v50, v50
	v_exp_f32_e32 v51, v51
	v_pk_add_f32 v[120:121], v[120:121], v[92:93]
	v_pk_add_f32 v[122:123], v[122:123], v[94:95]
	v_mfma_f32_32x32x64_f8f6f4 v[64:79], v[36:41], v[108:113], v[64:79] cbsz:2 blgp:2
	ds_read_b128 v[36:39], v124 offset:58368
	v_exp_f32_e32 v52, v52
	v_exp_f32_e32 v53, v53
	v_exp_f32_e32 v54, v54
	v_exp_f32_e32 v55, v55
	v_pk_add_f32 v[120:121], v[120:121], v[48:49]
	v_pk_add_f32 v[122:123], v[122:123], v[50:51]
	v_mfma_f32_32x32x64_f8f6f4 v[64:79], v[42:47], v[114:119], v[64:79] cbsz:2 blgp:2
	ds_read_b128 v[40:43], v124 offset:59392
	ds_read_b128 v[44:47], v124 offset:60416
	v_exp_f32_e32 v56, v56
	v_exp_f32_e32 v57, v57
	v_exp_f32_e32 v58, v58
	v_exp_f32_e32 v59, v59
	v_pk_add_f32 v[120:121], v[120:121], v[52:53]
	v_pk_add_f32 v[122:123], v[122:123], v[54:55]
	s_setprio 1
	s_waitcnt vmcnt(0) lgkmcnt(6)
	s_barrier
	v_mfma_f32_32x32x64_f8f6f4 v[80:95], v[0:5], v[96:101], 0 cbsz:2 blgp:2
	ds_read_b128 v[0:3], v124
	v_exp_f32_e32 v60, v60
	v_exp_f32_e32 v61, v61
	v_exp_f32_e32 v62, v62
	v_exp_f32_e32 v63, v63
	v_pk_add_f32 v[120:121], v[120:121], v[56:57]
	v_pk_add_f32 v[122:123], v[122:123], v[58:59]
	v_mfma_f32_32x32x64_f8f6f4 v[80:95], v[6:11], v[102:107], v[80:95] cbsz:2 blgp:2
	ds_read_b128 v[4:7], v124 offset:1024
	ds_read_b128 v[8:11], v124 offset:2048
	v_exp_f32_e32 v64, v64
	v_exp_f32_e32 v65, v65
	v_exp_f32_e32 v66, v66
	v_exp_f32_e32 v67, v67
	v_pk_add_f32 v[120:121], v[120:121], v[60:61]
	v_pk_add_f32 v[122:123], v[122:123], v[62:63]
	v_mfma_f32_32x32x64_f8f6f4 v[80:95], v[12:17], v[108:113], v[80:95] cbsz:2 blgp:2
	ds_read_b128 v[12:15], v124 offset:3072
	v_exp_f32_e32 v68, v68
	v_exp_f32_e32 v69, v69
	v_exp_f32_e32 v70, v70
	v_exp_f32_e32 v71, v71
	v_pk_add_f32 v[120:121], v[120:121], v[64:65]
	v_pk_add_f32 v[122:123], v[122:123], v[66:67]
	v_mfma_f32_32x32x64_f8f6f4 v[80:95], v[18:23], v[114:119], v[80:95] cbsz:2 blgp:2
	ds_read_b128 v[16:19], v124 offset:4096
	ds_read_b128 v[20:23], v124 offset:5120
	v_exp_f32_e32 v72, v72
	v_exp_f32_e32 v73, v73
	v_exp_f32_e32 v74, v74
	v_exp_f32_e32 v75, v75
	v_pk_add_f32 v[120:121], v[120:121], v[68:69]
	v_pk_add_f32 v[122:123], v[122:123], v[70:71]
	s_waitcnt lgkmcnt(6)
	v_mfma_f32_32x32x64_f8f6f4 v[48:63], v[24:29], v[96:101], 0 cbsz:2 blgp:2
	ds_read_b128 v[24:27], v124 offset:6144
	v_exp_f32_e32 v76, v76
	v_exp_f32_e32 v77, v77
	v_exp_f32_e32 v78, v78
	v_exp_f32_e32 v79, v79
	v_pk_add_f32 v[120:121], v[120:121], v[72:73]
	v_pk_add_f32 v[122:123], v[122:123], v[74:75]
	v_mfma_f32_32x32x64_f8f6f4 v[48:63], v[30:35], v[102:107], v[48:63] cbsz:2 blgp:2
	ds_read_b128 v[28:31], v124 offset:7168
	ds_read_b128 v[32:35], v124 offset:8192
	v_exp_f32_e32 v80, v80
	v_exp_f32_e32 v81, v81
	v_exp_f32_e32 v82, v82
	v_exp_f32_e32 v83, v83
	v_pk_add_f32 v[120:121], v[120:121], v[76:77]
	v_pk_add_f32 v[122:123], v[122:123], v[78:79]
	s_cmp_lg_u32 s8, 10
	s_cbranch_scc1 .Lmk_nosplit_b
	v_add_f32_e32 v127, v120, v121
	v_add_f32_e32 v126, v122, v123
	v_mov_b32_e32 v120, 0
	v_mov_b32_e32 v121, 0
	v_mov_b32_e32 v122, 0
	v_mov_b32_e32 v123, 0
	v_add_f32_e32 v127, v127, v126
